# P2 compress loop: loads of each trip issued together, two trips in flight (was one round trip per MFMA)
# speedup vs baseline: 1.0060x; 1.0001x over previous
.LBB0_380:
	s_and_b32 s9, s13, 0x60
	s_lshl_b32 s8, s26, 8
	v_or_b32_e32 v2, s9, v35
	s_and_b32 s8, s8, 0x7800
	v_min_u32_e32 v2, 0x7e, v2
	s_add_i32 s8, s10, s8
	v_lshlrev_b32_e32 v2, 4, v2
	v_add_u32_e32 v42, s8, v2
	s_ashr_i32 s8, s26, 7
	s_lshl_b32 s29, s26, 5
	s_ashr_i32 s9, s8, 31
	s_lshr_b32 s27, s26, 3
	s_lshr_b32 s28, s26, 2
	s_and_b32 s33, s29, 0x80
	s_lshl_b64 s[30:31], s[8:9], 23
	s_lshl_b64 s[34:35], s[8:9], 18
	v_lshl_add_u64 v[52:53], v[48:49], 0, s[34:35]
	s_add_u32 s34, s11, s33
	s_addc_u32 s35, s12, 0
	s_add_u32 s34, s34, s30
	v_lshlrev_b64 v[2:3], 8, v[42:43]
	s_addc_u32 s35, s35, s31
	v_lshl_add_u64 v[54:55], s[34:35], 0, v[2:3]
	s_add_u32 s34, s15, s33
	s_addc_u32 s35, s16, 0
	s_add_u32 s34, s34, s30
	s_addc_u32 s35, s35, s31
	v_lshl_add_u64 v[56:57], s[34:35], 0, v[2:3]
	s_add_u32 s34, s17, s33
	s_addc_u32 s35, s18, 0
	s_add_u32 s34, s34, s30
	s_addc_u32 s35, s35, s31
	s_add_u32 s33, s19, s33
	v_lshl_add_u64 v[58:59], s[34:35], 0, v[2:3]
	s_addc_u32 s34, s20, 0
	s_add_u32 s30, s33, s30
	s_addc_u32 s31, s34, s31
	v_lshl_add_u64 v[60:61], s[30:31], 0, v[2:3]
	s_mov_b32 s30, 16
	v_mov_b32_e32 v2, 0
	v_mov_b32_e32 v3, v43
	v_mov_b32_e32 v4, v43
	v_mov_b32_e32 v5, v43
	v_mov_b32_e32 v6, v43
	v_mov_b32_e32 v7, v43
	v_mov_b32_e32 v8, v43
	v_mov_b32_e32 v9, v43
	s_waitcnt vmcnt(0)
	v_mov_b32_e32 v10, v43
	v_mov_b32_e32 v11, v43
	v_mov_b32_e32 v12, v43
	v_mov_b32_e32 v13, v43
	v_mov_b32_e32 v14, v43
	v_mov_b32_e32 v15, v43
	v_mov_b32_e32 v16, v43
	v_mov_b32_e32 v17, v43
	v_mov_b32_e32 v18, 0
	v_mov_b32_e32 v19, v43
	v_mov_b32_e32 v20, v43
	v_mov_b32_e32 v21, v43
	v_mov_b32_e32 v22, v43
	v_mov_b32_e32 v23, v43
	v_mov_b32_e32 v24, v43
	v_mov_b32_e32 v25, v43
	v_mov_b32_e32 v26, v43
	v_mov_b32_e32 v27, v43
	v_mov_b32_e32 v28, v43
	v_mov_b32_e32 v29, v43
	v_mov_b32_e32 v30, v43
	v_mov_b32_e32 v31, v43
	v_mov_b32_e32 v32, v43
	v_mov_b32_e32 v33, v43
	v_lshl_add_u64 v[70:71], v[58:59], 0, v[46:47]
	global_load_dwordx4 v[92:95], v[70:71], off
	v_lshl_add_u64 v[70:71], v[60:61], 0, v[46:47]
	global_load_dwordx4 v[96:99], v[70:71], off
	v_lshl_add_u64 v[70:71], v[56:57], 0, v[46:47]
	global_load_dwordx4 v[100:103], v[70:71], off
	v_lshl_add_u64 v[70:71], v[54:55], 0, v[46:47]
	global_load_dwordx4 v[104:107], v[70:71], off
	v_lshl_add_u64 v[74:75], v[52:53], 0, v[46:47]
	v_add_co_u32_e32 v88, vcc, s21, v74
	s_nop 1
	v_addc_co_u32_e32 v89, vcc, 0, v75, vcc
	v_add_co_u32_e32 v90, vcc, s22, v74
	s_nop 1
	v_addc_co_u32_e32 v91, vcc, 0, v75, vcc
	global_load_dwordx4 v[108:111], v[88:89], off
	global_load_dwordx4 v[112:115], v[88:89], off offset:32
	global_load_dwordx4 v[116:119], v[88:89], off offset:64
	global_load_dwordx4 v[120:123], v[88:89], off offset:96
	global_load_dwordx4 v[124:127], v[90:91], off
	global_load_dwordx4 v[128:131], v[90:91], off offset:32
	global_load_dwordx4 v[132:135], v[90:91], off offset:64
	global_load_dwordx4 v[136:139], v[90:91], off offset:96
	v_lshl_add_u64 v[52:53], v[52:53], 0, s[4:5]
	v_lshl_add_u64 v[54:55], v[54:55], 0, s[6:7]
	v_lshl_add_u64 v[56:57], v[56:57], 0, s[6:7]
	v_lshl_add_u64 v[58:59], v[58:59], 0, s[6:7]
	v_lshl_add_u64 v[60:61], v[60:61], 0, s[6:7]
	v_lshl_add_u64 v[70:71], v[58:59], 0, v[46:47]
	global_load_dwordx4 v[140:143], v[70:71], off
	v_lshl_add_u64 v[70:71], v[60:61], 0, v[46:47]
	global_load_dwordx4 v[144:147], v[70:71], off
	v_lshl_add_u64 v[70:71], v[56:57], 0, v[46:47]
	global_load_dwordx4 v[148:151], v[70:71], off
	v_lshl_add_u64 v[70:71], v[54:55], 0, v[46:47]
	global_load_dwordx4 v[152:155], v[70:71], off
	v_lshl_add_u64 v[74:75], v[52:53], 0, v[46:47]
	v_add_co_u32_e32 v88, vcc, s21, v74
	s_nop 1
	v_addc_co_u32_e32 v89, vcc, 0, v75, vcc
	v_add_co_u32_e32 v90, vcc, s22, v74
	s_nop 1
	v_addc_co_u32_e32 v91, vcc, 0, v75, vcc
	global_load_dwordx4 v[156:159], v[88:89], off
	global_load_dwordx4 v[160:163], v[88:89], off offset:32
	global_load_dwordx4 v[164:167], v[88:89], off offset:64
	global_load_dwordx4 v[168:171], v[88:89], off offset:96
	global_load_dwordx4 v[172:175], v[90:91], off
	global_load_dwordx4 v[176:179], v[90:91], off offset:32
	global_load_dwordx4 v[180:183], v[90:91], off offset:64
	global_load_dwordx4 v[184:187], v[90:91], off offset:96
	v_lshl_add_u64 v[52:53], v[52:53], 0, s[4:5]
	v_lshl_add_u64 v[54:55], v[54:55], 0, s[6:7]
	v_lshl_add_u64 v[56:57], v[56:57], 0, s[6:7]
	v_lshl_add_u64 v[58:59], v[58:59], 0, s[6:7]
	v_lshl_add_u64 v[60:61], v[60:61], 0, s[6:7]
	s_waitcnt vmcnt(12)
	v_mfma_f32_32x32x16_bf16 v[2:17], v[92:95], v[108:111], v[2:17]
	v_mfma_f32_32x32x16_bf16 v[18:33], v[92:95], v[124:127], v[18:33]
	v_mfma_f32_32x32x16_bf16 v[2:17], v[96:99], v[112:115], v[2:17]
	v_mfma_f32_32x32x16_bf16 v[18:33], v[96:99], v[128:131], v[18:33]
	v_mfma_f32_32x32x16_bf16 v[2:17], v[100:103], v[116:119], v[2:17]
	v_mfma_f32_32x32x16_bf16 v[18:33], v[100:103], v[132:135], v[18:33]
	v_mfma_f32_32x32x16_bf16 v[2:17], v[104:107], v[120:123], v[2:17]
	v_mfma_f32_32x32x16_bf16 v[18:33], v[104:107], v[136:139], v[18:33]
	v_lshl_add_u64 v[70:71], v[58:59], 0, v[46:47]
	global_load_dwordx4 v[92:95], v[70:71], off
	v_lshl_add_u64 v[70:71], v[60:61], 0, v[46:47]
	global_load_dwordx4 v[96:99], v[70:71], off
	v_lshl_add_u64 v[70:71], v[56:57], 0, v[46:47]
	global_load_dwordx4 v[100:103], v[70:71], off
	v_lshl_add_u64 v[70:71], v[54:55], 0, v[46:47]
	global_load_dwordx4 v[104:107], v[70:71], off
	v_lshl_add_u64 v[74:75], v[52:53], 0, v[46:47]
	v_add_co_u32_e32 v88, vcc, s21, v74
	s_nop 1
	v_addc_co_u32_e32 v89, vcc, 0, v75, vcc
	v_add_co_u32_e32 v90, vcc, s22, v74
	s_nop 1
	v_addc_co_u32_e32 v91, vcc, 0, v75, vcc
	global_load_dwordx4 v[108:111], v[88:89], off
	global_load_dwordx4 v[112:115], v[88:89], off offset:32
	global_load_dwordx4 v[116:119], v[88:89], off offset:64
	global_load_dwordx4 v[120:123], v[88:89], off offset:96
	global_load_dwordx4 v[124:127], v[90:91], off
	global_load_dwordx4 v[128:131], v[90:91], off offset:32
	global_load_dwordx4 v[132:135], v[90:91], off offset:64
	global_load_dwordx4 v[136:139], v[90:91], off offset:96
	v_lshl_add_u64 v[52:53], v[52:53], 0, s[4:5]
	v_lshl_add_u64 v[54:55], v[54:55], 0, s[6:7]
	v_lshl_add_u64 v[56:57], v[56:57], 0, s[6:7]
	v_lshl_add_u64 v[58:59], v[58:59], 0, s[6:7]
	v_lshl_add_u64 v[60:61], v[60:61], 0, s[6:7]
	s_waitcnt vmcnt(12)
	v_mfma_f32_32x32x16_bf16 v[2:17], v[140:143], v[156:159], v[2:17]
	v_mfma_f32_32x32x16_bf16 v[18:33], v[140:143], v[172:175], v[18:33]
	v_mfma_f32_32x32x16_bf16 v[2:17], v[144:147], v[160:163], v[2:17]
	v_mfma_f32_32x32x16_bf16 v[18:33], v[144:147], v[176:179], v[18:33]
	v_mfma_f32_32x32x16_bf16 v[2:17], v[148:151], v[164:167], v[2:17]
	v_mfma_f32_32x32x16_bf16 v[18:33], v[148:151], v[180:183], v[18:33]
	v_mfma_f32_32x32x16_bf16 v[2:17], v[152:155], v[168:171], v[2:17]
	v_mfma_f32_32x32x16_bf16 v[18:33], v[152:155], v[184:187], v[18:33]
	v_lshl_add_u64 v[70:71], v[58:59], 0, v[46:47]
	global_load_dwordx4 v[140:143], v[70:71], off
	v_lshl_add_u64 v[70:71], v[60:61], 0, v[46:47]
	global_load_dwordx4 v[144:147], v[70:71], off
	v_lshl_add_u64 v[70:71], v[56:57], 0, v[46:47]
	global_load_dwordx4 v[148:151], v[70:71], off
	v_lshl_add_u64 v[70:71], v[54:55], 0, v[46:47]
	global_load_dwordx4 v[152:155], v[70:71], off
	v_lshl_add_u64 v[74:75], v[52:53], 0, v[46:47]
	v_add_co_u32_e32 v88, vcc, s21, v74
	s_nop 1
	v_addc_co_u32_e32 v89, vcc, 0, v75, vcc
	v_add_co_u32_e32 v90, vcc, s22, v74
	s_nop 1
	v_addc_co_u32_e32 v91, vcc, 0, v75, vcc
	global_load_dwordx4 v[156:159], v[88:89], off
	global_load_dwordx4 v[160:163], v[88:89], off offset:32
	global_load_dwordx4 v[164:167], v[88:89], off offset:64
	global_load_dwordx4 v[168:171], v[88:89], off offset:96
	global_load_dwordx4 v[172:175], v[90:91], off
	global_load_dwordx4 v[176:179], v[90:91], off offset:32
	global_load_dwordx4 v[180:183], v[90:91], off offset:64
	global_load_dwordx4 v[184:187], v[90:91], off offset:96
	v_lshl_add_u64 v[52:53], v[52:53], 0, s[4:5]
	v_lshl_add_u64 v[54:55], v[54:55], 0, s[6:7]
	v_lshl_add_u64 v[56:57], v[56:57], 0, s[6:7]
	v_lshl_add_u64 v[58:59], v[58:59], 0, s[6:7]
	v_lshl_add_u64 v[60:61], v[60:61], 0, s[6:7]
	s_waitcnt vmcnt(12)
	v_mfma_f32_32x32x16_bf16 v[2:17], v[92:95], v[108:111], v[2:17]
	v_mfma_f32_32x32x16_bf16 v[18:33], v[92:95], v[124:127], v[18:33]
	v_mfma_f32_32x32x16_bf16 v[2:17], v[96:99], v[112:115], v[2:17]
	v_mfma_f32_32x32x16_bf16 v[18:33], v[96:99], v[128:131], v[18:33]
	v_mfma_f32_32x32x16_bf16 v[2:17], v[100:103], v[116:119], v[2:17]
	v_mfma_f32_32x32x16_bf16 v[18:33], v[100:103], v[132:135], v[18:33]
	v_mfma_f32_32x32x16_bf16 v[2:17], v[104:107], v[120:123], v[2:17]
	v_mfma_f32_32x32x16_bf16 v[18:33], v[104:107], v[136:139], v[18:33]
	s_waitcnt vmcnt(0)
	v_mfma_f32_32x32x16_bf16 v[2:17], v[140:143], v[156:159], v[2:17]
	v_mfma_f32_32x32x16_bf16 v[18:33], v[140:143], v[172:175], v[18:33]
	v_mfma_f32_32x32x16_bf16 v[2:17], v[144:147], v[160:163], v[2:17]
	v_mfma_f32_32x32x16_bf16 v[18:33], v[144:147], v[176:179], v[18:33]
	v_mfma_f32_32x32x16_bf16 v[2:17], v[148:151], v[164:167], v[2:17]
	v_mfma_f32_32x32x16_bf16 v[18:33], v[148:151], v[180:183], v[18:33]
	v_mfma_f32_32x32x16_bf16 v[2:17], v[152:155], v[168:171], v[2:17]
	v_mfma_f32_32x32x16_bf16 v[18:33], v[152:155], v[184:187], v[18:33]
	s_lshl_b64 s[30:31], s[8:9], 14
	v_lshl_add_u64 v[52:53], v[44:45], 0, s[30:31]
	v_add_co_u32_e32 v56, vcc, 0x2000, v52
	s_nop 1
	v_addc_co_u32_e32 v57, vcc, 0, v53, vcc
	s_barrier
	global_load_dwordx4 v[52:55], v[52:53], off
	s_nop 0
	global_load_dwordx4 v[56:59], v[56:57], off
	s_lshl_b32 s8, s8, 6
	v_or_b32_e32 v60, s8, v40
	v_or_b32_e32 v70, s8, v65
	v_or_b32_e32 v72, s8, v66
	v_ashrrev_i32_e32 v61, 31, v60
	v_ashrrev_i32_e32 v71, 31, v70
	v_ashrrev_i32_e32 v73, 31, v72
	v_lshl_add_u64 v[60:61], v[60:61], 2, s[2:3]
	v_add_u32_e32 v42, 0x800, v39
	v_add_u32_e32 v51, 0x1000, v39
	v_add_u32_e32 v74, 0x1800, v39
	v_lshl_add_u64 v[70:71], v[70:71], 2, s[2:3]
	v_lshl_add_u64 v[72:73], v[72:73], 2, s[2:3]
	s_mov_b32 s8, 64
	s_waitcnt vmcnt(1)
	ds_write_b128 v41, v[52:55]
	s_waitcnt vmcnt(0)
	ds_write_b128 v62, v[56:59]
	ds_write2_b32 v39, v2, v18 offset1:32
	ds_write2_b32 v39, v3, v19 offset0:64 offset1:96
	ds_write2_b32 v39, v4, v20 offset0:128 offset1:160
	ds_write2_b32 v39, v5, v21 offset0:192 offset1:224
	ds_write2_b32 v42, v6, v22 offset1:32
	ds_write2_b32 v42, v7, v23 offset0:64 offset1:96
	ds_write2_b32 v42, v8, v24 offset0:128 offset1:160
	ds_write2_b32 v42, v9, v25 offset0:192 offset1:224
	ds_write2_b32 v51, v10, v26 offset1:32
	ds_write2_b32 v51, v11, v27 offset0:64 offset1:96
	ds_write2_b32 v51, v12, v28 offset0:128 offset1:160
	ds_write2_b32 v51, v13, v29 offset0:192 offset1:224
	ds_write2_b32 v74, v14, v30 offset1:32
	ds_write2_b32 v74, v15, v31 offset0:64 offset1:96
	ds_write2_b32 v74, v16, v32 offset0:128 offset1:160
	ds_write2_b32 v74, v17, v33 offset0:192 offset1:224
	s_waitcnt lgkmcnt(0)
	s_barrier
	global_load_dwordx2 v[32:33], v[60:61], off
	s_nop 0
	global_load_dword v60, v[70:71], off
	global_load_dword v61, v[72:73], off
	ds_read_b128 v[8:11], v63
	ds_read_b128 v[12:15], v63 offset:8192
	ds_read_b128 v[16:19], v63 offset:16384
	ds_read_b128 v[20:23], v63 offset:24576
	ds_read_b128 v[24:27], v63 offset:32768
	ds_read_b128 v[28:31], v63 offset:40960
	ds_read_b128 v[52:55], v63 offset:49152
	ds_read_b128 v[56:59], v63 offset:57344
	v_mov_b32_e32 v2, 0
	v_mov_b32_e32 v6, v68
	v_mov_b32_e32 v7, v69
	v_mov_b32_e32 v3, v2
	v_mov_b32_e32 v4, v2
	s_waitcnt vmcnt(2) lgkmcnt(7)
	v_pk_add_f32 v[8:9], v[32:33], v[8:9]
	s_waitcnt lgkmcnt(6)
	v_pk_add_f32 v[8:9], v[8:9], v[12:13]
	s_waitcnt vmcnt(0)
	v_pk_add_f32 v[10:11], v[60:61], v[10:11]
	s_waitcnt lgkmcnt(5)
	v_pk_add_f32 v[8:9], v[8:9], v[16:17]
	v_pk_add_f32 v[10:11], v[10:11], v[14:15]
	s_waitcnt lgkmcnt(4)
	v_pk_add_f32 v[8:9], v[8:9], v[20:21]
	v_pk_add_f32 v[10:11], v[10:11], v[18:19]
	s_waitcnt lgkmcnt(3)
	v_pk_add_f32 v[8:9], v[8:9], v[24:25]
	v_pk_add_f32 v[10:11], v[10:11], v[22:23]
	s_waitcnt lgkmcnt(2)
	v_pk_add_f32 v[8:9], v[8:9], v[28:29]
	v_pk_add_f32 v[10:11], v[10:11], v[26:27]
	s_waitcnt lgkmcnt(1)
	v_pk_add_f32 v[8:9], v[8:9], v[52:53]
	v_pk_add_f32 v[10:11], v[10:11], v[30:31]
	s_waitcnt lgkmcnt(0)
	v_pk_add_f32 v[8:9], v[8:9], v[56:57]
	v_pk_add_f32 v[10:11], v[10:11], v[54:55]
	v_mul_f32_e32 v5, 0x3d372713, v8
	v_pk_add_f32 v[10:11], v[10:11], v[58:59]
	v_mul_f32_e32 v12, 0x3d372713, v9
	v_mul_f32_e32 v13, 0x3d372713, v10
	v_mul_f32_e32 v14, 0x3d372713, v11
	v_mul_f32_e32 v5, v8, v5
	v_mul_f32_e32 v12, v9, v12
	v_mul_f32_e32 v13, v10, v13
	v_mul_f32_e32 v14, v11, v14
	v_fma_f32 v5, v8, v5, v8
	v_fma_f32 v12, v9, v12, v9
	v_fma_f32 v13, v10, v13, v10
	v_fma_f32 v14, v11, v14, v11
	v_mul_f32_e32 v5, 0x3f4c422a, v5
	v_mul_f32_e32 v12, 0x3f4c422a, v12
	v_mul_f32_e32 v13, 0x3f4c422a, v13
	v_mul_f32_e32 v14, 0x3f4c422a, v14
	v_mul_f32_e32 v5, 0x4038aa3b, v5
	v_mul_f32_e32 v12, 0x4038aa3b, v12
	v_mul_f32_e32 v13, 0x4038aa3b, v13
	v_mul_f32_e32 v14, 0x4038aa3b, v14
	v_exp_f32_e32 v5, v5
	v_exp_f32_e32 v12, v12
	v_exp_f32_e32 v13, v13
	v_exp_f32_e32 v14, v14
	v_add_f32_e32 v5, 1.0, v5
	v_add_f32_e32 v15, 1.0, v12
	v_add_f32_e32 v16, 1.0, v13
	v_add_f32_e32 v17, 1.0, v14
	v_rcp_f32_e32 v12, v5
	v_rcp_f32_e32 v13, v15
	v_rcp_f32_e32 v14, v16
	v_rcp_f32_e32 v15, v17
	v_pk_mul_f32 v[8:9], v[8:9], 0.5 op_sel_hi:[1,0]
	v_pk_fma_f32 v[12:13], v[12:13], 2.0, 1.0 op_sel_hi:[1,0,0] neg_lo:[1,0,0] neg_hi:[1,0,0]
	v_pk_mul_f32 v[10:11], v[10:11], 0.5 op_sel_hi:[1,0]
	v_pk_fma_f32 v[14:15], v[14:15], 2.0, 1.0 op_sel_hi:[1,0,0] neg_lo:[1,0,0] neg_hi:[1,0,0]
	v_pk_add_f32 v[12:13], v[12:13], 1.0 op_sel_hi:[1,0]
	v_pk_add_f32 v[14:15], v[14:15], 1.0 op_sel_hi:[1,0]
	v_pk_mul_f32 v[8:9], v[8:9], v[12:13]
	v_pk_mul_f32 v[10:11], v[10:11], v[14:15]
	v_mov_b32_e32 v5, v2
	ds_write_b128 v64, v[8:11]
	s_waitcnt lgkmcnt(0)
	s_barrier
